# combo7 + phase 10 rewritten: lane owns columns 256j+4l so every load/store instruction covers one contiguous span (full-line 1 KB stores), next token prefetched
# speedup vs baseline: 1.0133x; 1.0133x over previous
.LBB0_1219:
	s_cmp_lt_i32 s48, 11
	s_cselect_b64 s[6:7], -1, 0
	s_and_b64 s[4:5], s[6:7], s[4:5]
	s_andn2_b64 vcc, exec, s[4:5]
	s_cbranch_vccnz .LBB0_1225
	s_load_dwordx4 s[4:7], s[0:1], 0xa8
	v_and_b32_e32 v1, 63, v0
	v_lshrrev_b32_e32 v5, 6, v0
	s_lshl_b32 s13, s2, 3
	v_readfirstlane_b32 s12, v5
	v_lshlrev_b32_e32 v2, 2, v1
	v_lshlrev_b32_e32 v3, 3, v1
	v_lshlrev_b32_e32 v4, 4, v1
	s_add_i32 s12, s12, s13
	v_lshl_add_u32 v5, v1, 11, s12
	v_lshlrev_b32_e32 v5, 3, v5
	v_cmp_gt_u32_e32 vcc, 8, v1
	s_waitcnt lgkmcnt(0)
	s_add_u32 s8, s6, 0x33c0a000
	s_addc_u32 s9, s7, 0
	s_add_u32 s10, s6, 0x33c2a000
	s_addc_u32 s11, s7, 0
	s_add_u32 s48, s6, 0x4744a000
	s_addc_u32 s49, s7, 0
	s_add_u32 s60, s6, 0x2b80a000
	s_addc_u32 s61, s7, 0
	s_lshl_b32 s14, s12, 12
	s_add_u32 s62, s60, s14
	s_addc_u32 s63, s61, 0
	s_lshl_b32 s14, s12, 13
	s_add_u32 s64, s4, s14
	s_addc_u32 s65, s5, 0
	s_and_saveexec_b64 s[14:15], vcc
	global_load_dwordx2 v[6:7], v5, s[8:9]
	global_load_dwordx2 v[8:9], v5, s[10:11]
	s_waitcnt vmcnt(1)
	v_ashrrev_i32_e32 v10, 16, v6
	v_ashrrev_i32_e32 v11, 16, v7
	v_lshlrev_b32_e32 v10, 2, v10
	v_lshlrev_b32_e32 v11, 2, v11
	v_add_u32_e32 v10, 0x24140, v10
	v_add_u32_e32 v11, 0x24140, v11
	ds_read_b32 v10, v10
	ds_read_b32 v11, v11
	v_and_b32_e32 v6, 0xffff, v6
	v_and_b32_e32 v7, 0xffff, v7
	s_waitcnt lgkmcnt(0)
	v_lshl_add_u32 v6, v10, 8, v6
	v_lshl_add_u32 v7, v11, 8, v7
	s_waitcnt vmcnt(0)
	s_mov_b64 exec, s[14:15]
	s_nop 1
	v_readlane_b32 s16, v6, 0
	v_readlane_b32 s24, v7, 0
	v_readlane_b32 s32, v8, 0
	v_readlane_b32 s40, v9, 0
	v_readlane_b32 s17, v6, 1
	v_readlane_b32 s25, v7, 1
	v_readlane_b32 s33, v8, 1
	v_readlane_b32 s41, v9, 1
	v_readlane_b32 s18, v6, 2
	v_readlane_b32 s26, v7, 2
	v_readlane_b32 s34, v8, 2
	v_readlane_b32 s42, v9, 2
	v_readlane_b32 s19, v6, 3
	v_readlane_b32 s27, v7, 3
	v_readlane_b32 s35, v8, 3
	v_readlane_b32 s43, v9, 3
	v_readlane_b32 s20, v6, 4
	v_readlane_b32 s28, v7, 4
	v_readlane_b32 s36, v8, 4
	v_readlane_b32 s44, v9, 4
	v_readlane_b32 s21, v6, 5
	v_readlane_b32 s29, v7, 5
	v_readlane_b32 s37, v8, 5
	v_readlane_b32 s45, v9, 5
	v_readlane_b32 s22, v6, 6
	v_readlane_b32 s30, v7, 6
	v_readlane_b32 s38, v8, 6
	v_readlane_b32 s46, v9, 6
	v_readlane_b32 s23, v6, 7
	v_readlane_b32 s31, v7, 7
	v_readlane_b32 s39, v8, 7
	v_readlane_b32 s47, v9, 7
	s_nop 3
	s_lshl_b32 s50, s16, 11
	s_add_u32 s50, s48, s50
	s_addc_u32 s51, s49, 0
	s_lshl_b32 s52, s24, 11
	s_add_u32 s52, s48, s52
	s_addc_u32 s53, s49, 0
	s_mov_b64 s[54:55], s[62:63]
	global_load_dword v64, v2, s[50:51]
	global_load_dword v65, v2, s[50:51] offset:256
	global_load_dword v66, v2, s[50:51] offset:512
	global_load_dword v67, v2, s[50:51] offset:768
	global_load_dword v68, v2, s[50:51] offset:1024
	global_load_dword v69, v2, s[50:51] offset:1280
	global_load_dword v70, v2, s[50:51] offset:1536
	global_load_dword v71, v2, s[50:51] offset:1792
	global_load_dword v72, v2, s[52:53]
	global_load_dword v73, v2, s[52:53] offset:256
	global_load_dword v74, v2, s[52:53] offset:512
	global_load_dword v75, v2, s[52:53] offset:768
	global_load_dword v76, v2, s[52:53] offset:1024
	global_load_dword v77, v2, s[52:53] offset:1280
	global_load_dword v78, v2, s[52:53] offset:1536
	global_load_dword v79, v2, s[52:53] offset:1792
	global_load_dwordx2 v[80:81], v3, s[54:55]
	global_load_dwordx2 v[82:83], v3, s[54:55] offset:512
	global_load_dwordx2 v[84:85], v3, s[54:55] offset:1024
	global_load_dwordx2 v[86:87], v3, s[54:55] offset:1536
	global_load_dwordx2 v[88:89], v3, s[54:55] offset:2048
	global_load_dwordx2 v[90:91], v3, s[54:55] offset:2560
	global_load_dwordx2 v[92:93], v3, s[54:55] offset:3072
	global_load_dwordx2 v[94:95], v3, s[54:55] offset:3584
	s_waitcnt vmcnt(0)
	s_lshl_b32 s50, s17, 11
	s_add_u32 s50, s48, s50
	s_addc_u32 s51, s49, 0
	s_lshl_b32 s52, s25, 11
	s_add_u32 s52, s48, s52
	s_addc_u32 s53, s49, 0
	s_add_u32 s54, s62, 0x800000
	s_addc_u32 s55, s63, 0
	global_load_dword v96, v2, s[50:51]
	global_load_dword v97, v2, s[50:51] offset:256
	global_load_dword v98, v2, s[50:51] offset:512
	global_load_dword v99, v2, s[50:51] offset:768
	global_load_dword v100, v2, s[50:51] offset:1024
	global_load_dword v101, v2, s[50:51] offset:1280
	global_load_dword v102, v2, s[50:51] offset:1536
	global_load_dword v103, v2, s[50:51] offset:1792
	global_load_dword v104, v2, s[52:53]
	global_load_dword v105, v2, s[52:53] offset:256
	global_load_dword v106, v2, s[52:53] offset:512
	global_load_dword v107, v2, s[52:53] offset:768
	global_load_dword v108, v2, s[52:53] offset:1024
	global_load_dword v109, v2, s[52:53] offset:1280
	global_load_dword v110, v2, s[52:53] offset:1536
	global_load_dword v111, v2, s[52:53] offset:1792
	global_load_dwordx2 v[112:113], v3, s[54:55]
	global_load_dwordx2 v[114:115], v3, s[54:55] offset:512
	global_load_dwordx2 v[116:117], v3, s[54:55] offset:1024
	global_load_dwordx2 v[118:119], v3, s[54:55] offset:1536
	global_load_dwordx2 v[120:121], v3, s[54:55] offset:2048
	global_load_dwordx2 v[122:123], v3, s[54:55] offset:2560
	global_load_dwordx2 v[124:125], v3, s[54:55] offset:3072
	global_load_dwordx2 v[126:127], v3, s[54:55] offset:3584
	v_mov_b32_e32 v240, s32
	v_mov_b32_e32 v242, s40
	v_cvt_pk_f32_fp8_e32 v[224:225], v64
	v_cvt_pk_f32_fp8_sdwa v[226:227], v64 src0_sel:WORD_1
	v_cvt_pk_f32_fp8_e32 v[228:229], v72
	v_cvt_pk_f32_fp8_sdwa v[230:231], v72 src0_sel:WORD_1
	v_lshlrev_b32_e32 v192, 16, v80
	v_and_b32_e32 v193, 0xffff0000, v80
	v_lshlrev_b32_e32 v194, 16, v81
	v_and_b32_e32 v195, 0xffff0000, v81
	v_pk_fma_f32 v[192:193], v[224:225], v[240:241], v[192:193] op_sel_hi:[1,0,1]
	v_pk_fma_f32 v[194:195], v[226:227], v[240:241], v[194:195] op_sel_hi:[1,0,1]
	v_pk_fma_f32 v[192:193], v[228:229], v[242:243], v[192:193] op_sel_hi:[1,0,1]
	v_pk_fma_f32 v[194:195], v[230:231], v[242:243], v[194:195] op_sel_hi:[1,0,1]
	v_cvt_pk_f32_fp8_e32 v[232:233], v65
	v_cvt_pk_f32_fp8_sdwa v[234:235], v65 src0_sel:WORD_1
	v_cvt_pk_f32_fp8_e32 v[236:237], v73
	v_cvt_pk_f32_fp8_sdwa v[238:239], v73 src0_sel:WORD_1
	v_lshlrev_b32_e32 v196, 16, v82
	v_and_b32_e32 v197, 0xffff0000, v82
	v_lshlrev_b32_e32 v198, 16, v83
	v_and_b32_e32 v199, 0xffff0000, v83
	v_pk_fma_f32 v[196:197], v[232:233], v[240:241], v[196:197] op_sel_hi:[1,0,1]
	v_pk_fma_f32 v[198:199], v[234:235], v[240:241], v[198:199] op_sel_hi:[1,0,1]
	v_pk_fma_f32 v[196:197], v[236:237], v[242:243], v[196:197] op_sel_hi:[1,0,1]
	v_pk_fma_f32 v[198:199], v[238:239], v[242:243], v[198:199] op_sel_hi:[1,0,1]
	v_cvt_pk_f32_fp8_e32 v[224:225], v66
	v_cvt_pk_f32_fp8_sdwa v[226:227], v66 src0_sel:WORD_1
	v_cvt_pk_f32_fp8_e32 v[228:229], v74
	v_cvt_pk_f32_fp8_sdwa v[230:231], v74 src0_sel:WORD_1
	v_lshlrev_b32_e32 v200, 16, v84
	v_and_b32_e32 v201, 0xffff0000, v84
	v_lshlrev_b32_e32 v202, 16, v85
	v_and_b32_e32 v203, 0xffff0000, v85
	v_pk_fma_f32 v[200:201], v[224:225], v[240:241], v[200:201] op_sel_hi:[1,0,1]
	v_pk_fma_f32 v[202:203], v[226:227], v[240:241], v[202:203] op_sel_hi:[1,0,1]
	v_pk_fma_f32 v[200:201], v[228:229], v[242:243], v[200:201] op_sel_hi:[1,0,1]
	v_pk_fma_f32 v[202:203], v[230:231], v[242:243], v[202:203] op_sel_hi:[1,0,1]
	v_cvt_pk_f32_fp8_e32 v[232:233], v67
	v_cvt_pk_f32_fp8_sdwa v[234:235], v67 src0_sel:WORD_1
	v_cvt_pk_f32_fp8_e32 v[236:237], v75
	v_cvt_pk_f32_fp8_sdwa v[238:239], v75 src0_sel:WORD_1
	v_lshlrev_b32_e32 v204, 16, v86
	v_and_b32_e32 v205, 0xffff0000, v86
	v_lshlrev_b32_e32 v206, 16, v87
	v_and_b32_e32 v207, 0xffff0000, v87
	v_pk_fma_f32 v[204:205], v[232:233], v[240:241], v[204:205] op_sel_hi:[1,0,1]
	v_pk_fma_f32 v[206:207], v[234:235], v[240:241], v[206:207] op_sel_hi:[1,0,1]
	v_pk_fma_f32 v[204:205], v[236:237], v[242:243], v[204:205] op_sel_hi:[1,0,1]
	v_pk_fma_f32 v[206:207], v[238:239], v[242:243], v[206:207] op_sel_hi:[1,0,1]
	v_cvt_pk_f32_fp8_e32 v[224:225], v68
	v_cvt_pk_f32_fp8_sdwa v[226:227], v68 src0_sel:WORD_1
	v_cvt_pk_f32_fp8_e32 v[228:229], v76
	v_cvt_pk_f32_fp8_sdwa v[230:231], v76 src0_sel:WORD_1
	v_lshlrev_b32_e32 v208, 16, v88
	v_and_b32_e32 v209, 0xffff0000, v88
	v_lshlrev_b32_e32 v210, 16, v89
	v_and_b32_e32 v211, 0xffff0000, v89
	v_pk_fma_f32 v[208:209], v[224:225], v[240:241], v[208:209] op_sel_hi:[1,0,1]
	v_pk_fma_f32 v[210:211], v[226:227], v[240:241], v[210:211] op_sel_hi:[1,0,1]
	v_pk_fma_f32 v[208:209], v[228:229], v[242:243], v[208:209] op_sel_hi:[1,0,1]
	v_pk_fma_f32 v[210:211], v[230:231], v[242:243], v[210:211] op_sel_hi:[1,0,1]
	v_cvt_pk_f32_fp8_e32 v[232:233], v69
	v_cvt_pk_f32_fp8_sdwa v[234:235], v69 src0_sel:WORD_1
	v_cvt_pk_f32_fp8_e32 v[236:237], v77
	v_cvt_pk_f32_fp8_sdwa v[238:239], v77 src0_sel:WORD_1
	v_lshlrev_b32_e32 v212, 16, v90
	v_and_b32_e32 v213, 0xffff0000, v90
	v_lshlrev_b32_e32 v214, 16, v91
	v_and_b32_e32 v215, 0xffff0000, v91
	v_pk_fma_f32 v[212:213], v[232:233], v[240:241], v[212:213] op_sel_hi:[1,0,1]
	v_pk_fma_f32 v[214:215], v[234:235], v[240:241], v[214:215] op_sel_hi:[1,0,1]
	v_pk_fma_f32 v[212:213], v[236:237], v[242:243], v[212:213] op_sel_hi:[1,0,1]
	v_pk_fma_f32 v[214:215], v[238:239], v[242:243], v[214:215] op_sel_hi:[1,0,1]
	v_cvt_pk_f32_fp8_e32 v[224:225], v70
	v_cvt_pk_f32_fp8_sdwa v[226:227], v70 src0_sel:WORD_1
	v_cvt_pk_f32_fp8_e32 v[228:229], v78
	v_cvt_pk_f32_fp8_sdwa v[230:231], v78 src0_sel:WORD_1
	v_lshlrev_b32_e32 v216, 16, v92
	v_and_b32_e32 v217, 0xffff0000, v92
	v_lshlrev_b32_e32 v218, 16, v93
	v_and_b32_e32 v219, 0xffff0000, v93
	v_pk_fma_f32 v[216:217], v[224:225], v[240:241], v[216:217] op_sel_hi:[1,0,1]
	v_pk_fma_f32 v[218:219], v[226:227], v[240:241], v[218:219] op_sel_hi:[1,0,1]
	v_pk_fma_f32 v[216:217], v[228:229], v[242:243], v[216:217] op_sel_hi:[1,0,1]
	v_pk_fma_f32 v[218:219], v[230:231], v[242:243], v[218:219] op_sel_hi:[1,0,1]
	v_cvt_pk_f32_fp8_e32 v[232:233], v71
	v_cvt_pk_f32_fp8_sdwa v[234:235], v71 src0_sel:WORD_1
	v_cvt_pk_f32_fp8_e32 v[236:237], v79
	v_cvt_pk_f32_fp8_sdwa v[238:239], v79 src0_sel:WORD_1
	v_lshlrev_b32_e32 v220, 16, v94
	v_and_b32_e32 v221, 0xffff0000, v94
	v_lshlrev_b32_e32 v222, 16, v95
	v_and_b32_e32 v223, 0xffff0000, v95
	v_pk_fma_f32 v[220:221], v[232:233], v[240:241], v[220:221] op_sel_hi:[1,0,1]
	v_pk_fma_f32 v[222:223], v[234:235], v[240:241], v[222:223] op_sel_hi:[1,0,1]
	v_pk_fma_f32 v[220:221], v[236:237], v[242:243], v[220:221] op_sel_hi:[1,0,1]
	v_pk_fma_f32 v[222:223], v[238:239], v[242:243], v[222:223] op_sel_hi:[1,0,1]
	s_mov_b64 s[56:57], s[64:65]
	s_add_u32 s58, s56, 0x1000
	s_addc_u32 s59, s57, 0
	global_store_dwordx4 v4, v[192:195], s[56:57]
	global_store_dwordx4 v4, v[196:199], s[56:57] offset:1024
	global_store_dwordx4 v4, v[200:203], s[56:57] offset:2048
	global_store_dwordx4 v4, v[204:207], s[56:57] offset:3072
	global_store_dwordx4 v4, v[208:211], s[58:59]
	global_store_dwordx4 v4, v[212:215], s[58:59] offset:1024
	global_store_dwordx4 v4, v[216:219], s[58:59] offset:2048
	global_store_dwordx4 v4, v[220:223], s[58:59] offset:3072
	s_waitcnt vmcnt(8)
	s_lshl_b32 s50, s18, 11
	s_add_u32 s50, s48, s50
	s_addc_u32 s51, s49, 0
	s_lshl_b32 s52, s26, 11
	s_add_u32 s52, s48, s52
	s_addc_u32 s53, s49, 0
	s_add_u32 s54, s62, 0x1000000
	s_addc_u32 s55, s63, 0
	global_load_dword v64, v2, s[50:51]
	global_load_dword v65, v2, s[50:51] offset:256
	global_load_dword v66, v2, s[50:51] offset:512
	global_load_dword v67, v2, s[50:51] offset:768
	global_load_dword v68, v2, s[50:51] offset:1024
	global_load_dword v69, v2, s[50:51] offset:1280
	global_load_dword v70, v2, s[50:51] offset:1536
	global_load_dword v71, v2, s[50:51] offset:1792
	global_load_dword v72, v2, s[52:53]
	global_load_dword v73, v2, s[52:53] offset:256
	global_load_dword v74, v2, s[52:53] offset:512
	global_load_dword v75, v2, s[52:53] offset:768
	global_load_dword v76, v2, s[52:53] offset:1024
	global_load_dword v77, v2, s[52:53] offset:1280
	global_load_dword v78, v2, s[52:53] offset:1536
	global_load_dword v79, v2, s[52:53] offset:1792
	global_load_dwordx2 v[80:81], v3, s[54:55]
	global_load_dwordx2 v[82:83], v3, s[54:55] offset:512
	global_load_dwordx2 v[84:85], v3, s[54:55] offset:1024
	global_load_dwordx2 v[86:87], v3, s[54:55] offset:1536
	global_load_dwordx2 v[88:89], v3, s[54:55] offset:2048
	global_load_dwordx2 v[90:91], v3, s[54:55] offset:2560
	global_load_dwordx2 v[92:93], v3, s[54:55] offset:3072
	global_load_dwordx2 v[94:95], v3, s[54:55] offset:3584
	v_mov_b32_e32 v240, s33
	v_mov_b32_e32 v242, s41
	v_cvt_pk_f32_fp8_e32 v[224:225], v96
	v_cvt_pk_f32_fp8_sdwa v[226:227], v96 src0_sel:WORD_1
	v_cvt_pk_f32_fp8_e32 v[228:229], v104
	v_cvt_pk_f32_fp8_sdwa v[230:231], v104 src0_sel:WORD_1
	v_lshlrev_b32_e32 v192, 16, v112
	v_and_b32_e32 v193, 0xffff0000, v112
	v_lshlrev_b32_e32 v194, 16, v113
	v_and_b32_e32 v195, 0xffff0000, v113
	v_pk_fma_f32 v[192:193], v[224:225], v[240:241], v[192:193] op_sel_hi:[1,0,1]
	v_pk_fma_f32 v[194:195], v[226:227], v[240:241], v[194:195] op_sel_hi:[1,0,1]
	v_pk_fma_f32 v[192:193], v[228:229], v[242:243], v[192:193] op_sel_hi:[1,0,1]
	v_pk_fma_f32 v[194:195], v[230:231], v[242:243], v[194:195] op_sel_hi:[1,0,1]
	v_cvt_pk_f32_fp8_e32 v[232:233], v97
	v_cvt_pk_f32_fp8_sdwa v[234:235], v97 src0_sel:WORD_1
	v_cvt_pk_f32_fp8_e32 v[236:237], v105
	v_cvt_pk_f32_fp8_sdwa v[238:239], v105 src0_sel:WORD_1
	v_lshlrev_b32_e32 v196, 16, v114
	v_and_b32_e32 v197, 0xffff0000, v114
	v_lshlrev_b32_e32 v198, 16, v115
	v_and_b32_e32 v199, 0xffff0000, v115
	v_pk_fma_f32 v[196:197], v[232:233], v[240:241], v[196:197] op_sel_hi:[1,0,1]
	v_pk_fma_f32 v[198:199], v[234:235], v[240:241], v[198:199] op_sel_hi:[1,0,1]
	v_pk_fma_f32 v[196:197], v[236:237], v[242:243], v[196:197] op_sel_hi:[1,0,1]
	v_pk_fma_f32 v[198:199], v[238:239], v[242:243], v[198:199] op_sel_hi:[1,0,1]
	v_cvt_pk_f32_fp8_e32 v[224:225], v98
	v_cvt_pk_f32_fp8_sdwa v[226:227], v98 src0_sel:WORD_1
	v_cvt_pk_f32_fp8_e32 v[228:229], v106
	v_cvt_pk_f32_fp8_sdwa v[230:231], v106 src0_sel:WORD_1
	v_lshlrev_b32_e32 v200, 16, v116
	v_and_b32_e32 v201, 0xffff0000, v116
	v_lshlrev_b32_e32 v202, 16, v117
	v_and_b32_e32 v203, 0xffff0000, v117
	v_pk_fma_f32 v[200:201], v[224:225], v[240:241], v[200:201] op_sel_hi:[1,0,1]
	v_pk_fma_f32 v[202:203], v[226:227], v[240:241], v[202:203] op_sel_hi:[1,0,1]
	v_pk_fma_f32 v[200:201], v[228:229], v[242:243], v[200:201] op_sel_hi:[1,0,1]
	v_pk_fma_f32 v[202:203], v[230:231], v[242:243], v[202:203] op_sel_hi:[1,0,1]
	v_cvt_pk_f32_fp8_e32 v[232:233], v99
	v_cvt_pk_f32_fp8_sdwa v[234:235], v99 src0_sel:WORD_1
	v_cvt_pk_f32_fp8_e32 v[236:237], v107
	v_cvt_pk_f32_fp8_sdwa v[238:239], v107 src0_sel:WORD_1
	v_lshlrev_b32_e32 v204, 16, v118
	v_and_b32_e32 v205, 0xffff0000, v118
	v_lshlrev_b32_e32 v206, 16, v119
	v_and_b32_e32 v207, 0xffff0000, v119
	v_pk_fma_f32 v[204:205], v[232:233], v[240:241], v[204:205] op_sel_hi:[1,0,1]
	v_pk_fma_f32 v[206:207], v[234:235], v[240:241], v[206:207] op_sel_hi:[1,0,1]
	v_pk_fma_f32 v[204:205], v[236:237], v[242:243], v[204:205] op_sel_hi:[1,0,1]
	v_pk_fma_f32 v[206:207], v[238:239], v[242:243], v[206:207] op_sel_hi:[1,0,1]
	v_cvt_pk_f32_fp8_e32 v[224:225], v100
	v_cvt_pk_f32_fp8_sdwa v[226:227], v100 src0_sel:WORD_1
	v_cvt_pk_f32_fp8_e32 v[228:229], v108
	v_cvt_pk_f32_fp8_sdwa v[230:231], v108 src0_sel:WORD_1
	v_lshlrev_b32_e32 v208, 16, v120
	v_and_b32_e32 v209, 0xffff0000, v120
	v_lshlrev_b32_e32 v210, 16, v121
	v_and_b32_e32 v211, 0xffff0000, v121
	v_pk_fma_f32 v[208:209], v[224:225], v[240:241], v[208:209] op_sel_hi:[1,0,1]
	v_pk_fma_f32 v[210:211], v[226:227], v[240:241], v[210:211] op_sel_hi:[1,0,1]
	v_pk_fma_f32 v[208:209], v[228:229], v[242:243], v[208:209] op_sel_hi:[1,0,1]
	v_pk_fma_f32 v[210:211], v[230:231], v[242:243], v[210:211] op_sel_hi:[1,0,1]
	v_cvt_pk_f32_fp8_e32 v[232:233], v101
	v_cvt_pk_f32_fp8_sdwa v[234:235], v101 src0_sel:WORD_1
	v_cvt_pk_f32_fp8_e32 v[236:237], v109
	v_cvt_pk_f32_fp8_sdwa v[238:239], v109 src0_sel:WORD_1
	v_lshlrev_b32_e32 v212, 16, v122
	v_and_b32_e32 v213, 0xffff0000, v122
	v_lshlrev_b32_e32 v214, 16, v123
	v_and_b32_e32 v215, 0xffff0000, v123
	v_pk_fma_f32 v[212:213], v[232:233], v[240:241], v[212:213] op_sel_hi:[1,0,1]
	v_pk_fma_f32 v[214:215], v[234:235], v[240:241], v[214:215] op_sel_hi:[1,0,1]
	v_pk_fma_f32 v[212:213], v[236:237], v[242:243], v[212:213] op_sel_hi:[1,0,1]
	v_pk_fma_f32 v[214:215], v[238:239], v[242:243], v[214:215] op_sel_hi:[1,0,1]
	v_cvt_pk_f32_fp8_e32 v[224:225], v102
	v_cvt_pk_f32_fp8_sdwa v[226:227], v102 src0_sel:WORD_1
	v_cvt_pk_f32_fp8_e32 v[228:229], v110
	v_cvt_pk_f32_fp8_sdwa v[230:231], v110 src0_sel:WORD_1
	v_lshlrev_b32_e32 v216, 16, v124
	v_and_b32_e32 v217, 0xffff0000, v124
	v_lshlrev_b32_e32 v218, 16, v125
	v_and_b32_e32 v219, 0xffff0000, v125
	v_pk_fma_f32 v[216:217], v[224:225], v[240:241], v[216:217] op_sel_hi:[1,0,1]
	v_pk_fma_f32 v[218:219], v[226:227], v[240:241], v[218:219] op_sel_hi:[1,0,1]
	v_pk_fma_f32 v[216:217], v[228:229], v[242:243], v[216:217] op_sel_hi:[1,0,1]
	v_pk_fma_f32 v[218:219], v[230:231], v[242:243], v[218:219] op_sel_hi:[1,0,1]
	v_cvt_pk_f32_fp8_e32 v[232:233], v103
	v_cvt_pk_f32_fp8_sdwa v[234:235], v103 src0_sel:WORD_1
	v_cvt_pk_f32_fp8_e32 v[236:237], v111
	v_cvt_pk_f32_fp8_sdwa v[238:239], v111 src0_sel:WORD_1
	v_lshlrev_b32_e32 v220, 16, v126
	v_and_b32_e32 v221, 0xffff0000, v126
	v_lshlrev_b32_e32 v222, 16, v127
	v_and_b32_e32 v223, 0xffff0000, v127
	v_pk_fma_f32 v[220:221], v[232:233], v[240:241], v[220:221] op_sel_hi:[1,0,1]
	v_pk_fma_f32 v[222:223], v[234:235], v[240:241], v[222:223] op_sel_hi:[1,0,1]
	v_pk_fma_f32 v[220:221], v[236:237], v[242:243], v[220:221] op_sel_hi:[1,0,1]
	v_pk_fma_f32 v[222:223], v[238:239], v[242:243], v[222:223] op_sel_hi:[1,0,1]
	s_add_u32 s56, s64, 0x1000000
	s_addc_u32 s57, s65, 0
	s_add_u32 s58, s56, 0x1000
	s_addc_u32 s59, s57, 0
	global_store_dwordx4 v4, v[192:195], s[56:57]
	global_store_dwordx4 v4, v[196:199], s[56:57] offset:1024
	global_store_dwordx4 v4, v[200:203], s[56:57] offset:2048
	global_store_dwordx4 v4, v[204:207], s[56:57] offset:3072
	global_store_dwordx4 v4, v[208:211], s[58:59]
	global_store_dwordx4 v4, v[212:215], s[58:59] offset:1024
	global_store_dwordx4 v4, v[216:219], s[58:59] offset:2048
	global_store_dwordx4 v4, v[220:223], s[58:59] offset:3072
	s_waitcnt vmcnt(8)
	s_lshl_b32 s50, s19, 11
	s_add_u32 s50, s48, s50
	s_addc_u32 s51, s49, 0
	s_lshl_b32 s52, s27, 11
	s_add_u32 s52, s48, s52
	s_addc_u32 s53, s49, 0
	s_add_u32 s54, s62, 0x1800000
	s_addc_u32 s55, s63, 0
	global_load_dword v96, v2, s[50:51]
	global_load_dword v97, v2, s[50:51] offset:256
	global_load_dword v98, v2, s[50:51] offset:512
	global_load_dword v99, v2, s[50:51] offset:768
	global_load_dword v100, v2, s[50:51] offset:1024
	global_load_dword v101, v2, s[50:51] offset:1280
	global_load_dword v102, v2, s[50:51] offset:1536
	global_load_dword v103, v2, s[50:51] offset:1792
	global_load_dword v104, v2, s[52:53]
	global_load_dword v105, v2, s[52:53] offset:256
	global_load_dword v106, v2, s[52:53] offset:512
	global_load_dword v107, v2, s[52:53] offset:768
	global_load_dword v108, v2, s[52:53] offset:1024
	global_load_dword v109, v2, s[52:53] offset:1280
	global_load_dword v110, v2, s[52:53] offset:1536
	global_load_dword v111, v2, s[52:53] offset:1792
	global_load_dwordx2 v[112:113], v3, s[54:55]
	global_load_dwordx2 v[114:115], v3, s[54:55] offset:512
	global_load_dwordx2 v[116:117], v3, s[54:55] offset:1024
	global_load_dwordx2 v[118:119], v3, s[54:55] offset:1536
	global_load_dwordx2 v[120:121], v3, s[54:55] offset:2048
	global_load_dwordx2 v[122:123], v3, s[54:55] offset:2560
	global_load_dwordx2 v[124:125], v3, s[54:55] offset:3072
	global_load_dwordx2 v[126:127], v3, s[54:55] offset:3584
	v_mov_b32_e32 v240, s34
	v_mov_b32_e32 v242, s42
	v_cvt_pk_f32_fp8_e32 v[224:225], v64
	v_cvt_pk_f32_fp8_sdwa v[226:227], v64 src0_sel:WORD_1
	v_cvt_pk_f32_fp8_e32 v[228:229], v72
	v_cvt_pk_f32_fp8_sdwa v[230:231], v72 src0_sel:WORD_1
	v_lshlrev_b32_e32 v192, 16, v80
	v_and_b32_e32 v193, 0xffff0000, v80
	v_lshlrev_b32_e32 v194, 16, v81
	v_and_b32_e32 v195, 0xffff0000, v81
	v_pk_fma_f32 v[192:193], v[224:225], v[240:241], v[192:193] op_sel_hi:[1,0,1]
	v_pk_fma_f32 v[194:195], v[226:227], v[240:241], v[194:195] op_sel_hi:[1,0,1]
	v_pk_fma_f32 v[192:193], v[228:229], v[242:243], v[192:193] op_sel_hi:[1,0,1]
	v_pk_fma_f32 v[194:195], v[230:231], v[242:243], v[194:195] op_sel_hi:[1,0,1]
	v_cvt_pk_f32_fp8_e32 v[232:233], v65
	v_cvt_pk_f32_fp8_sdwa v[234:235], v65 src0_sel:WORD_1
	v_cvt_pk_f32_fp8_e32 v[236:237], v73
	v_cvt_pk_f32_fp8_sdwa v[238:239], v73 src0_sel:WORD_1
	v_lshlrev_b32_e32 v196, 16, v82
	v_and_b32_e32 v197, 0xffff0000, v82
	v_lshlrev_b32_e32 v198, 16, v83
	v_and_b32_e32 v199, 0xffff0000, v83
	v_pk_fma_f32 v[196:197], v[232:233], v[240:241], v[196:197] op_sel_hi:[1,0,1]
	v_pk_fma_f32 v[198:199], v[234:235], v[240:241], v[198:199] op_sel_hi:[1,0,1]
	v_pk_fma_f32 v[196:197], v[236:237], v[242:243], v[196:197] op_sel_hi:[1,0,1]
	v_pk_fma_f32 v[198:199], v[238:239], v[242:243], v[198:199] op_sel_hi:[1,0,1]
	v_cvt_pk_f32_fp8_e32 v[224:225], v66
	v_cvt_pk_f32_fp8_sdwa v[226:227], v66 src0_sel:WORD_1
	v_cvt_pk_f32_fp8_e32 v[228:229], v74
	v_cvt_pk_f32_fp8_sdwa v[230:231], v74 src0_sel:WORD_1
	v_lshlrev_b32_e32 v200, 16, v84
	v_and_b32_e32 v201, 0xffff0000, v84
	v_lshlrev_b32_e32 v202, 16, v85
	v_and_b32_e32 v203, 0xffff0000, v85
	v_pk_fma_f32 v[200:201], v[224:225], v[240:241], v[200:201] op_sel_hi:[1,0,1]
	v_pk_fma_f32 v[202:203], v[226:227], v[240:241], v[202:203] op_sel_hi:[1,0,1]
	v_pk_fma_f32 v[200:201], v[228:229], v[242:243], v[200:201] op_sel_hi:[1,0,1]
	v_pk_fma_f32 v[202:203], v[230:231], v[242:243], v[202:203] op_sel_hi:[1,0,1]
	v_cvt_pk_f32_fp8_e32 v[232:233], v67
	v_cvt_pk_f32_fp8_sdwa v[234:235], v67 src0_sel:WORD_1
	v_cvt_pk_f32_fp8_e32 v[236:237], v75
	v_cvt_pk_f32_fp8_sdwa v[238:239], v75 src0_sel:WORD_1
	v_lshlrev_b32_e32 v204, 16, v86
	v_and_b32_e32 v205, 0xffff0000, v86
	v_lshlrev_b32_e32 v206, 16, v87
	v_and_b32_e32 v207, 0xffff0000, v87
	v_pk_fma_f32 v[204:205], v[232:233], v[240:241], v[204:205] op_sel_hi:[1,0,1]
	v_pk_fma_f32 v[206:207], v[234:235], v[240:241], v[206:207] op_sel_hi:[1,0,1]
	v_pk_fma_f32 v[204:205], v[236:237], v[242:243], v[204:205] op_sel_hi:[1,0,1]
	v_pk_fma_f32 v[206:207], v[238:239], v[242:243], v[206:207] op_sel_hi:[1,0,1]
	v_cvt_pk_f32_fp8_e32 v[224:225], v68
	v_cvt_pk_f32_fp8_sdwa v[226:227], v68 src0_sel:WORD_1
	v_cvt_pk_f32_fp8_e32 v[228:229], v76
	v_cvt_pk_f32_fp8_sdwa v[230:231], v76 src0_sel:WORD_1
	v_lshlrev_b32_e32 v208, 16, v88
	v_and_b32_e32 v209, 0xffff0000, v88
	v_lshlrev_b32_e32 v210, 16, v89
	v_and_b32_e32 v211, 0xffff0000, v89
	v_pk_fma_f32 v[208:209], v[224:225], v[240:241], v[208:209] op_sel_hi:[1,0,1]
	v_pk_fma_f32 v[210:211], v[226:227], v[240:241], v[210:211] op_sel_hi:[1,0,1]
	v_pk_fma_f32 v[208:209], v[228:229], v[242:243], v[208:209] op_sel_hi:[1,0,1]
	v_pk_fma_f32 v[210:211], v[230:231], v[242:243], v[210:211] op_sel_hi:[1,0,1]
	v_cvt_pk_f32_fp8_e32 v[232:233], v69
	v_cvt_pk_f32_fp8_sdwa v[234:235], v69 src0_sel:WORD_1
	v_cvt_pk_f32_fp8_e32 v[236:237], v77
	v_cvt_pk_f32_fp8_sdwa v[238:239], v77 src0_sel:WORD_1
	v_lshlrev_b32_e32 v212, 16, v90
	v_and_b32_e32 v213, 0xffff0000, v90
	v_lshlrev_b32_e32 v214, 16, v91
	v_and_b32_e32 v215, 0xffff0000, v91
	v_pk_fma_f32 v[212:213], v[232:233], v[240:241], v[212:213] op_sel_hi:[1,0,1]
	v_pk_fma_f32 v[214:215], v[234:235], v[240:241], v[214:215] op_sel_hi:[1,0,1]
	v_pk_fma_f32 v[212:213], v[236:237], v[242:243], v[212:213] op_sel_hi:[1,0,1]
	v_pk_fma_f32 v[214:215], v[238:239], v[242:243], v[214:215] op_sel_hi:[1,0,1]
	v_cvt_pk_f32_fp8_e32 v[224:225], v70
	v_cvt_pk_f32_fp8_sdwa v[226:227], v70 src0_sel:WORD_1
	v_cvt_pk_f32_fp8_e32 v[228:229], v78
	v_cvt_pk_f32_fp8_sdwa v[230:231], v78 src0_sel:WORD_1
	v_lshlrev_b32_e32 v216, 16, v92
	v_and_b32_e32 v217, 0xffff0000, v92
	v_lshlrev_b32_e32 v218, 16, v93
	v_and_b32_e32 v219, 0xffff0000, v93
	v_pk_fma_f32 v[216:217], v[224:225], v[240:241], v[216:217] op_sel_hi:[1,0,1]
	v_pk_fma_f32 v[218:219], v[226:227], v[240:241], v[218:219] op_sel_hi:[1,0,1]
	v_pk_fma_f32 v[216:217], v[228:229], v[242:243], v[216:217] op_sel_hi:[1,0,1]
	v_pk_fma_f32 v[218:219], v[230:231], v[242:243], v[218:219] op_sel_hi:[1,0,1]
	v_cvt_pk_f32_fp8_e32 v[232:233], v71
	v_cvt_pk_f32_fp8_sdwa v[234:235], v71 src0_sel:WORD_1
	v_cvt_pk_f32_fp8_e32 v[236:237], v79
	v_cvt_pk_f32_fp8_sdwa v[238:239], v79 src0_sel:WORD_1
	v_lshlrev_b32_e32 v220, 16, v94
	v_and_b32_e32 v221, 0xffff0000, v94
	v_lshlrev_b32_e32 v222, 16, v95
	v_and_b32_e32 v223, 0xffff0000, v95
	v_pk_fma_f32 v[220:221], v[232:233], v[240:241], v[220:221] op_sel_hi:[1,0,1]
	v_pk_fma_f32 v[222:223], v[234:235], v[240:241], v[222:223] op_sel_hi:[1,0,1]
	v_pk_fma_f32 v[220:221], v[236:237], v[242:243], v[220:221] op_sel_hi:[1,0,1]
	v_pk_fma_f32 v[222:223], v[238:239], v[242:243], v[222:223] op_sel_hi:[1,0,1]
	s_add_u32 s56, s64, 0x2000000
	s_addc_u32 s57, s65, 0
	s_add_u32 s58, s56, 0x1000
	s_addc_u32 s59, s57, 0
	global_store_dwordx4 v4, v[192:195], s[56:57]
	global_store_dwordx4 v4, v[196:199], s[56:57] offset:1024
	global_store_dwordx4 v4, v[200:203], s[56:57] offset:2048
	global_store_dwordx4 v4, v[204:207], s[56:57] offset:3072
	global_store_dwordx4 v4, v[208:211], s[58:59]
	global_store_dwordx4 v4, v[212:215], s[58:59] offset:1024
	global_store_dwordx4 v4, v[216:219], s[58:59] offset:2048
	global_store_dwordx4 v4, v[220:223], s[58:59] offset:3072
	s_waitcnt vmcnt(8)
	s_lshl_b32 s50, s20, 11
	s_add_u32 s50, s48, s50
	s_addc_u32 s51, s49, 0
	s_lshl_b32 s52, s28, 11
	s_add_u32 s52, s48, s52
	s_addc_u32 s53, s49, 0
	s_add_u32 s54, s62, 0x2000000
	s_addc_u32 s55, s63, 0
	global_load_dword v64, v2, s[50:51]
	global_load_dword v65, v2, s[50:51] offset:256
	global_load_dword v66, v2, s[50:51] offset:512
	global_load_dword v67, v2, s[50:51] offset:768
	global_load_dword v68, v2, s[50:51] offset:1024
	global_load_dword v69, v2, s[50:51] offset:1280
	global_load_dword v70, v2, s[50:51] offset:1536
	global_load_dword v71, v2, s[50:51] offset:1792
	global_load_dword v72, v2, s[52:53]
	global_load_dword v73, v2, s[52:53] offset:256
	global_load_dword v74, v2, s[52:53] offset:512
	global_load_dword v75, v2, s[52:53] offset:768
	global_load_dword v76, v2, s[52:53] offset:1024
	global_load_dword v77, v2, s[52:53] offset:1280
	global_load_dword v78, v2, s[52:53] offset:1536
	global_load_dword v79, v2, s[52:53] offset:1792
	global_load_dwordx2 v[80:81], v3, s[54:55]
	global_load_dwordx2 v[82:83], v3, s[54:55] offset:512
	global_load_dwordx2 v[84:85], v3, s[54:55] offset:1024
	global_load_dwordx2 v[86:87], v3, s[54:55] offset:1536
	global_load_dwordx2 v[88:89], v3, s[54:55] offset:2048
	global_load_dwordx2 v[90:91], v3, s[54:55] offset:2560
	global_load_dwordx2 v[92:93], v3, s[54:55] offset:3072
	global_load_dwordx2 v[94:95], v3, s[54:55] offset:3584
	v_mov_b32_e32 v240, s35
	v_mov_b32_e32 v242, s43
	v_cvt_pk_f32_fp8_e32 v[224:225], v96
	v_cvt_pk_f32_fp8_sdwa v[226:227], v96 src0_sel:WORD_1
	v_cvt_pk_f32_fp8_e32 v[228:229], v104
	v_cvt_pk_f32_fp8_sdwa v[230:231], v104 src0_sel:WORD_1
	v_lshlrev_b32_e32 v192, 16, v112
	v_and_b32_e32 v193, 0xffff0000, v112
	v_lshlrev_b32_e32 v194, 16, v113
	v_and_b32_e32 v195, 0xffff0000, v113
	v_pk_fma_f32 v[192:193], v[224:225], v[240:241], v[192:193] op_sel_hi:[1,0,1]
	v_pk_fma_f32 v[194:195], v[226:227], v[240:241], v[194:195] op_sel_hi:[1,0,1]
	v_pk_fma_f32 v[192:193], v[228:229], v[242:243], v[192:193] op_sel_hi:[1,0,1]
	v_pk_fma_f32 v[194:195], v[230:231], v[242:243], v[194:195] op_sel_hi:[1,0,1]
	v_cvt_pk_f32_fp8_e32 v[232:233], v97
	v_cvt_pk_f32_fp8_sdwa v[234:235], v97 src0_sel:WORD_1
	v_cvt_pk_f32_fp8_e32 v[236:237], v105
	v_cvt_pk_f32_fp8_sdwa v[238:239], v105 src0_sel:WORD_1
	v_lshlrev_b32_e32 v196, 16, v114
	v_and_b32_e32 v197, 0xffff0000, v114
	v_lshlrev_b32_e32 v198, 16, v115
	v_and_b32_e32 v199, 0xffff0000, v115
	v_pk_fma_f32 v[196:197], v[232:233], v[240:241], v[196:197] op_sel_hi:[1,0,1]
	v_pk_fma_f32 v[198:199], v[234:235], v[240:241], v[198:199] op_sel_hi:[1,0,1]
	v_pk_fma_f32 v[196:197], v[236:237], v[242:243], v[196:197] op_sel_hi:[1,0,1]
	v_pk_fma_f32 v[198:199], v[238:239], v[242:243], v[198:199] op_sel_hi:[1,0,1]
	v_cvt_pk_f32_fp8_e32 v[224:225], v98
	v_cvt_pk_f32_fp8_sdwa v[226:227], v98 src0_sel:WORD_1
	v_cvt_pk_f32_fp8_e32 v[228:229], v106
	v_cvt_pk_f32_fp8_sdwa v[230:231], v106 src0_sel:WORD_1
	v_lshlrev_b32_e32 v200, 16, v116
	v_and_b32_e32 v201, 0xffff0000, v116
	v_lshlrev_b32_e32 v202, 16, v117
	v_and_b32_e32 v203, 0xffff0000, v117
	v_pk_fma_f32 v[200:201], v[224:225], v[240:241], v[200:201] op_sel_hi:[1,0,1]
	v_pk_fma_f32 v[202:203], v[226:227], v[240:241], v[202:203] op_sel_hi:[1,0,1]
	v_pk_fma_f32 v[200:201], v[228:229], v[242:243], v[200:201] op_sel_hi:[1,0,1]
	v_pk_fma_f32 v[202:203], v[230:231], v[242:243], v[202:203] op_sel_hi:[1,0,1]
	v_cvt_pk_f32_fp8_e32 v[232:233], v99
	v_cvt_pk_f32_fp8_sdwa v[234:235], v99 src0_sel:WORD_1
	v_cvt_pk_f32_fp8_e32 v[236:237], v107
	v_cvt_pk_f32_fp8_sdwa v[238:239], v107 src0_sel:WORD_1
	v_lshlrev_b32_e32 v204, 16, v118
	v_and_b32_e32 v205, 0xffff0000, v118
	v_lshlrev_b32_e32 v206, 16, v119
	v_and_b32_e32 v207, 0xffff0000, v119
	v_pk_fma_f32 v[204:205], v[232:233], v[240:241], v[204:205] op_sel_hi:[1,0,1]
	v_pk_fma_f32 v[206:207], v[234:235], v[240:241], v[206:207] op_sel_hi:[1,0,1]
	v_pk_fma_f32 v[204:205], v[236:237], v[242:243], v[204:205] op_sel_hi:[1,0,1]
	v_pk_fma_f32 v[206:207], v[238:239], v[242:243], v[206:207] op_sel_hi:[1,0,1]
	v_cvt_pk_f32_fp8_e32 v[224:225], v100
	v_cvt_pk_f32_fp8_sdwa v[226:227], v100 src0_sel:WORD_1
	v_cvt_pk_f32_fp8_e32 v[228:229], v108
	v_cvt_pk_f32_fp8_sdwa v[230:231], v108 src0_sel:WORD_1
	v_lshlrev_b32_e32 v208, 16, v120
	v_and_b32_e32 v209, 0xffff0000, v120
	v_lshlrev_b32_e32 v210, 16, v121
	v_and_b32_e32 v211, 0xffff0000, v121
	v_pk_fma_f32 v[208:209], v[224:225], v[240:241], v[208:209] op_sel_hi:[1,0,1]
	v_pk_fma_f32 v[210:211], v[226:227], v[240:241], v[210:211] op_sel_hi:[1,0,1]
	v_pk_fma_f32 v[208:209], v[228:229], v[242:243], v[208:209] op_sel_hi:[1,0,1]
	v_pk_fma_f32 v[210:211], v[230:231], v[242:243], v[210:211] op_sel_hi:[1,0,1]
	v_cvt_pk_f32_fp8_e32 v[232:233], v101
	v_cvt_pk_f32_fp8_sdwa v[234:235], v101 src0_sel:WORD_1
	v_cvt_pk_f32_fp8_e32 v[236:237], v109
	v_cvt_pk_f32_fp8_sdwa v[238:239], v109 src0_sel:WORD_1
	v_lshlrev_b32_e32 v212, 16, v122
	v_and_b32_e32 v213, 0xffff0000, v122
	v_lshlrev_b32_e32 v214, 16, v123
	v_and_b32_e32 v215, 0xffff0000, v123
	v_pk_fma_f32 v[212:213], v[232:233], v[240:241], v[212:213] op_sel_hi:[1,0,1]
	v_pk_fma_f32 v[214:215], v[234:235], v[240:241], v[214:215] op_sel_hi:[1,0,1]
	v_pk_fma_f32 v[212:213], v[236:237], v[242:243], v[212:213] op_sel_hi:[1,0,1]
	v_pk_fma_f32 v[214:215], v[238:239], v[242:243], v[214:215] op_sel_hi:[1,0,1]
	v_cvt_pk_f32_fp8_e32 v[224:225], v102
	v_cvt_pk_f32_fp8_sdwa v[226:227], v102 src0_sel:WORD_1
	v_cvt_pk_f32_fp8_e32 v[228:229], v110
	v_cvt_pk_f32_fp8_sdwa v[230:231], v110 src0_sel:WORD_1
	v_lshlrev_b32_e32 v216, 16, v124
	v_and_b32_e32 v217, 0xffff0000, v124
	v_lshlrev_b32_e32 v218, 16, v125
	v_and_b32_e32 v219, 0xffff0000, v125
	v_pk_fma_f32 v[216:217], v[224:225], v[240:241], v[216:217] op_sel_hi:[1,0,1]
	v_pk_fma_f32 v[218:219], v[226:227], v[240:241], v[218:219] op_sel_hi:[1,0,1]
	v_pk_fma_f32 v[216:217], v[228:229], v[242:243], v[216:217] op_sel_hi:[1,0,1]
	v_pk_fma_f32 v[218:219], v[230:231], v[242:243], v[218:219] op_sel_hi:[1,0,1]
	v_cvt_pk_f32_fp8_e32 v[232:233], v103
	v_cvt_pk_f32_fp8_sdwa v[234:235], v103 src0_sel:WORD_1
	v_cvt_pk_f32_fp8_e32 v[236:237], v111
	v_cvt_pk_f32_fp8_sdwa v[238:239], v111 src0_sel:WORD_1
	v_lshlrev_b32_e32 v220, 16, v126
	v_and_b32_e32 v221, 0xffff0000, v126
	v_lshlrev_b32_e32 v222, 16, v127
	v_and_b32_e32 v223, 0xffff0000, v127
	v_pk_fma_f32 v[220:221], v[232:233], v[240:241], v[220:221] op_sel_hi:[1,0,1]
	v_pk_fma_f32 v[222:223], v[234:235], v[240:241], v[222:223] op_sel_hi:[1,0,1]
	v_pk_fma_f32 v[220:221], v[236:237], v[242:243], v[220:221] op_sel_hi:[1,0,1]
	v_pk_fma_f32 v[222:223], v[238:239], v[242:243], v[222:223] op_sel_hi:[1,0,1]
	s_add_u32 s56, s64, 0x3000000
	s_addc_u32 s57, s65, 0
	s_add_u32 s58, s56, 0x1000
	s_addc_u32 s59, s57, 0
	global_store_dwordx4 v4, v[192:195], s[56:57]
	global_store_dwordx4 v4, v[196:199], s[56:57] offset:1024
	global_store_dwordx4 v4, v[200:203], s[56:57] offset:2048
	global_store_dwordx4 v4, v[204:207], s[56:57] offset:3072
	global_store_dwordx4 v4, v[208:211], s[58:59]
	global_store_dwordx4 v4, v[212:215], s[58:59] offset:1024
	global_store_dwordx4 v4, v[216:219], s[58:59] offset:2048
	global_store_dwordx4 v4, v[220:223], s[58:59] offset:3072
	s_waitcnt vmcnt(8)
	s_lshl_b32 s50, s21, 11
	s_add_u32 s50, s48, s50
	s_addc_u32 s51, s49, 0
	s_lshl_b32 s52, s29, 11
	s_add_u32 s52, s48, s52
	s_addc_u32 s53, s49, 0
	s_add_u32 s54, s62, 0x2800000
	s_addc_u32 s55, s63, 0
	global_load_dword v96, v2, s[50:51]
	global_load_dword v97, v2, s[50:51] offset:256
	global_load_dword v98, v2, s[50:51] offset:512
	global_load_dword v99, v2, s[50:51] offset:768
	global_load_dword v100, v2, s[50:51] offset:1024
	global_load_dword v101, v2, s[50:51] offset:1280
	global_load_dword v102, v2, s[50:51] offset:1536
	global_load_dword v103, v2, s[50:51] offset:1792
	global_load_dword v104, v2, s[52:53]
	global_load_dword v105, v2, s[52:53] offset:256
	global_load_dword v106, v2, s[52:53] offset:512
	global_load_dword v107, v2, s[52:53] offset:768
	global_load_dword v108, v2, s[52:53] offset:1024
	global_load_dword v109, v2, s[52:53] offset:1280
	global_load_dword v110, v2, s[52:53] offset:1536
	global_load_dword v111, v2, s[52:53] offset:1792
	global_load_dwordx2 v[112:113], v3, s[54:55]
	global_load_dwordx2 v[114:115], v3, s[54:55] offset:512
	global_load_dwordx2 v[116:117], v3, s[54:55] offset:1024
	global_load_dwordx2 v[118:119], v3, s[54:55] offset:1536
	global_load_dwordx2 v[120:121], v3, s[54:55] offset:2048
	global_load_dwordx2 v[122:123], v3, s[54:55] offset:2560
	global_load_dwordx2 v[124:125], v3, s[54:55] offset:3072
	global_load_dwordx2 v[126:127], v3, s[54:55] offset:3584
	v_mov_b32_e32 v240, s36
	v_mov_b32_e32 v242, s44
	v_cvt_pk_f32_fp8_e32 v[224:225], v64
	v_cvt_pk_f32_fp8_sdwa v[226:227], v64 src0_sel:WORD_1
	v_cvt_pk_f32_fp8_e32 v[228:229], v72
	v_cvt_pk_f32_fp8_sdwa v[230:231], v72 src0_sel:WORD_1
	v_lshlrev_b32_e32 v192, 16, v80
	v_and_b32_e32 v193, 0xffff0000, v80
	v_lshlrev_b32_e32 v194, 16, v81
	v_and_b32_e32 v195, 0xffff0000, v81
	v_pk_fma_f32 v[192:193], v[224:225], v[240:241], v[192:193] op_sel_hi:[1,0,1]
	v_pk_fma_f32 v[194:195], v[226:227], v[240:241], v[194:195] op_sel_hi:[1,0,1]
	v_pk_fma_f32 v[192:193], v[228:229], v[242:243], v[192:193] op_sel_hi:[1,0,1]
	v_pk_fma_f32 v[194:195], v[230:231], v[242:243], v[194:195] op_sel_hi:[1,0,1]
	v_cvt_pk_f32_fp8_e32 v[232:233], v65
	v_cvt_pk_f32_fp8_sdwa v[234:235], v65 src0_sel:WORD_1
	v_cvt_pk_f32_fp8_e32 v[236:237], v73
	v_cvt_pk_f32_fp8_sdwa v[238:239], v73 src0_sel:WORD_1
	v_lshlrev_b32_e32 v196, 16, v82
	v_and_b32_e32 v197, 0xffff0000, v82
	v_lshlrev_b32_e32 v198, 16, v83
	v_and_b32_e32 v199, 0xffff0000, v83
	v_pk_fma_f32 v[196:197], v[232:233], v[240:241], v[196:197] op_sel_hi:[1,0,1]
	v_pk_fma_f32 v[198:199], v[234:235], v[240:241], v[198:199] op_sel_hi:[1,0,1]
	v_pk_fma_f32 v[196:197], v[236:237], v[242:243], v[196:197] op_sel_hi:[1,0,1]
	v_pk_fma_f32 v[198:199], v[238:239], v[242:243], v[198:199] op_sel_hi:[1,0,1]
	v_cvt_pk_f32_fp8_e32 v[224:225], v66
	v_cvt_pk_f32_fp8_sdwa v[226:227], v66 src0_sel:WORD_1
	v_cvt_pk_f32_fp8_e32 v[228:229], v74
	v_cvt_pk_f32_fp8_sdwa v[230:231], v74 src0_sel:WORD_1
	v_lshlrev_b32_e32 v200, 16, v84
	v_and_b32_e32 v201, 0xffff0000, v84
	v_lshlrev_b32_e32 v202, 16, v85
	v_and_b32_e32 v203, 0xffff0000, v85
	v_pk_fma_f32 v[200:201], v[224:225], v[240:241], v[200:201] op_sel_hi:[1,0,1]
	v_pk_fma_f32 v[202:203], v[226:227], v[240:241], v[202:203] op_sel_hi:[1,0,1]
	v_pk_fma_f32 v[200:201], v[228:229], v[242:243], v[200:201] op_sel_hi:[1,0,1]
	v_pk_fma_f32 v[202:203], v[230:231], v[242:243], v[202:203] op_sel_hi:[1,0,1]
	v_cvt_pk_f32_fp8_e32 v[232:233], v67
	v_cvt_pk_f32_fp8_sdwa v[234:235], v67 src0_sel:WORD_1
	v_cvt_pk_f32_fp8_e32 v[236:237], v75
	v_cvt_pk_f32_fp8_sdwa v[238:239], v75 src0_sel:WORD_1
	v_lshlrev_b32_e32 v204, 16, v86
	v_and_b32_e32 v205, 0xffff0000, v86
	v_lshlrev_b32_e32 v206, 16, v87
	v_and_b32_e32 v207, 0xffff0000, v87
	v_pk_fma_f32 v[204:205], v[232:233], v[240:241], v[204:205] op_sel_hi:[1,0,1]
	v_pk_fma_f32 v[206:207], v[234:235], v[240:241], v[206:207] op_sel_hi:[1,0,1]
	v_pk_fma_f32 v[204:205], v[236:237], v[242:243], v[204:205] op_sel_hi:[1,0,1]
	v_pk_fma_f32 v[206:207], v[238:239], v[242:243], v[206:207] op_sel_hi:[1,0,1]
	v_cvt_pk_f32_fp8_e32 v[224:225], v68
	v_cvt_pk_f32_fp8_sdwa v[226:227], v68 src0_sel:WORD_1
	v_cvt_pk_f32_fp8_e32 v[228:229], v76
	v_cvt_pk_f32_fp8_sdwa v[230:231], v76 src0_sel:WORD_1
	v_lshlrev_b32_e32 v208, 16, v88
	v_and_b32_e32 v209, 0xffff0000, v88
	v_lshlrev_b32_e32 v210, 16, v89
	v_and_b32_e32 v211, 0xffff0000, v89
	v_pk_fma_f32 v[208:209], v[224:225], v[240:241], v[208:209] op_sel_hi:[1,0,1]
	v_pk_fma_f32 v[210:211], v[226:227], v[240:241], v[210:211] op_sel_hi:[1,0,1]
	v_pk_fma_f32 v[208:209], v[228:229], v[242:243], v[208:209] op_sel_hi:[1,0,1]
	v_pk_fma_f32 v[210:211], v[230:231], v[242:243], v[210:211] op_sel_hi:[1,0,1]
	v_cvt_pk_f32_fp8_e32 v[232:233], v69
	v_cvt_pk_f32_fp8_sdwa v[234:235], v69 src0_sel:WORD_1
	v_cvt_pk_f32_fp8_e32 v[236:237], v77
	v_cvt_pk_f32_fp8_sdwa v[238:239], v77 src0_sel:WORD_1
	v_lshlrev_b32_e32 v212, 16, v90
	v_and_b32_e32 v213, 0xffff0000, v90
	v_lshlrev_b32_e32 v214, 16, v91
	v_and_b32_e32 v215, 0xffff0000, v91
	v_pk_fma_f32 v[212:213], v[232:233], v[240:241], v[212:213] op_sel_hi:[1,0,1]
	v_pk_fma_f32 v[214:215], v[234:235], v[240:241], v[214:215] op_sel_hi:[1,0,1]
	v_pk_fma_f32 v[212:213], v[236:237], v[242:243], v[212:213] op_sel_hi:[1,0,1]
	v_pk_fma_f32 v[214:215], v[238:239], v[242:243], v[214:215] op_sel_hi:[1,0,1]
	v_cvt_pk_f32_fp8_e32 v[224:225], v70
	v_cvt_pk_f32_fp8_sdwa v[226:227], v70 src0_sel:WORD_1
	v_cvt_pk_f32_fp8_e32 v[228:229], v78
	v_cvt_pk_f32_fp8_sdwa v[230:231], v78 src0_sel:WORD_1
	v_lshlrev_b32_e32 v216, 16, v92
	v_and_b32_e32 v217, 0xffff0000, v92
	v_lshlrev_b32_e32 v218, 16, v93
	v_and_b32_e32 v219, 0xffff0000, v93
	v_pk_fma_f32 v[216:217], v[224:225], v[240:241], v[216:217] op_sel_hi:[1,0,1]
	v_pk_fma_f32 v[218:219], v[226:227], v[240:241], v[218:219] op_sel_hi:[1,0,1]
	v_pk_fma_f32 v[216:217], v[228:229], v[242:243], v[216:217] op_sel_hi:[1,0,1]
	v_pk_fma_f32 v[218:219], v[230:231], v[242:243], v[218:219] op_sel_hi:[1,0,1]
	v_cvt_pk_f32_fp8_e32 v[232:233], v71
	v_cvt_pk_f32_fp8_sdwa v[234:235], v71 src0_sel:WORD_1
	v_cvt_pk_f32_fp8_e32 v[236:237], v79
	v_cvt_pk_f32_fp8_sdwa v[238:239], v79 src0_sel:WORD_1
	v_lshlrev_b32_e32 v220, 16, v94
	v_and_b32_e32 v221, 0xffff0000, v94
	v_lshlrev_b32_e32 v222, 16, v95
	v_and_b32_e32 v223, 0xffff0000, v95
	v_pk_fma_f32 v[220:221], v[232:233], v[240:241], v[220:221] op_sel_hi:[1,0,1]
	v_pk_fma_f32 v[222:223], v[234:235], v[240:241], v[222:223] op_sel_hi:[1,0,1]
	v_pk_fma_f32 v[220:221], v[236:237], v[242:243], v[220:221] op_sel_hi:[1,0,1]
	v_pk_fma_f32 v[222:223], v[238:239], v[242:243], v[222:223] op_sel_hi:[1,0,1]
	s_add_u32 s56, s64, 0x4000000
	s_addc_u32 s57, s65, 0
	s_add_u32 s58, s56, 0x1000
	s_addc_u32 s59, s57, 0
	global_store_dwordx4 v4, v[192:195], s[56:57]
	global_store_dwordx4 v4, v[196:199], s[56:57] offset:1024
	global_store_dwordx4 v4, v[200:203], s[56:57] offset:2048
	global_store_dwordx4 v4, v[204:207], s[56:57] offset:3072
	global_store_dwordx4 v4, v[208:211], s[58:59]
	global_store_dwordx4 v4, v[212:215], s[58:59] offset:1024
	global_store_dwordx4 v4, v[216:219], s[58:59] offset:2048
	global_store_dwordx4 v4, v[220:223], s[58:59] offset:3072
	s_waitcnt vmcnt(8)
	s_lshl_b32 s50, s22, 11
	s_add_u32 s50, s48, s50
	s_addc_u32 s51, s49, 0
	s_lshl_b32 s52, s30, 11
	s_add_u32 s52, s48, s52
	s_addc_u32 s53, s49, 0
	s_add_u32 s54, s62, 0x3000000
	s_addc_u32 s55, s63, 0
	global_load_dword v64, v2, s[50:51]
	global_load_dword v65, v2, s[50:51] offset:256
	global_load_dword v66, v2, s[50:51] offset:512
	global_load_dword v67, v2, s[50:51] offset:768
	global_load_dword v68, v2, s[50:51] offset:1024
	global_load_dword v69, v2, s[50:51] offset:1280
	global_load_dword v70, v2, s[50:51] offset:1536
	global_load_dword v71, v2, s[50:51] offset:1792
	global_load_dword v72, v2, s[52:53]
	global_load_dword v73, v2, s[52:53] offset:256
	global_load_dword v74, v2, s[52:53] offset:512
	global_load_dword v75, v2, s[52:53] offset:768
	global_load_dword v76, v2, s[52:53] offset:1024
	global_load_dword v77, v2, s[52:53] offset:1280
	global_load_dword v78, v2, s[52:53] offset:1536
	global_load_dword v79, v2, s[52:53] offset:1792
	global_load_dwordx2 v[80:81], v3, s[54:55]
	global_load_dwordx2 v[82:83], v3, s[54:55] offset:512
	global_load_dwordx2 v[84:85], v3, s[54:55] offset:1024
	global_load_dwordx2 v[86:87], v3, s[54:55] offset:1536
	global_load_dwordx2 v[88:89], v3, s[54:55] offset:2048
	global_load_dwordx2 v[90:91], v3, s[54:55] offset:2560
	global_load_dwordx2 v[92:93], v3, s[54:55] offset:3072
	global_load_dwordx2 v[94:95], v3, s[54:55] offset:3584
	v_mov_b32_e32 v240, s37
	v_mov_b32_e32 v242, s45
	v_cvt_pk_f32_fp8_e32 v[224:225], v96
	v_cvt_pk_f32_fp8_sdwa v[226:227], v96 src0_sel:WORD_1
	v_cvt_pk_f32_fp8_e32 v[228:229], v104
	v_cvt_pk_f32_fp8_sdwa v[230:231], v104 src0_sel:WORD_1
	v_lshlrev_b32_e32 v192, 16, v112
	v_and_b32_e32 v193, 0xffff0000, v112
	v_lshlrev_b32_e32 v194, 16, v113
	v_and_b32_e32 v195, 0xffff0000, v113
	v_pk_fma_f32 v[192:193], v[224:225], v[240:241], v[192:193] op_sel_hi:[1,0,1]
	v_pk_fma_f32 v[194:195], v[226:227], v[240:241], v[194:195] op_sel_hi:[1,0,1]
	v_pk_fma_f32 v[192:193], v[228:229], v[242:243], v[192:193] op_sel_hi:[1,0,1]
	v_pk_fma_f32 v[194:195], v[230:231], v[242:243], v[194:195] op_sel_hi:[1,0,1]
	v_cvt_pk_f32_fp8_e32 v[232:233], v97
	v_cvt_pk_f32_fp8_sdwa v[234:235], v97 src0_sel:WORD_1
	v_cvt_pk_f32_fp8_e32 v[236:237], v105
	v_cvt_pk_f32_fp8_sdwa v[238:239], v105 src0_sel:WORD_1
	v_lshlrev_b32_e32 v196, 16, v114
	v_and_b32_e32 v197, 0xffff0000, v114
	v_lshlrev_b32_e32 v198, 16, v115
	v_and_b32_e32 v199, 0xffff0000, v115
	v_pk_fma_f32 v[196:197], v[232:233], v[240:241], v[196:197] op_sel_hi:[1,0,1]
	v_pk_fma_f32 v[198:199], v[234:235], v[240:241], v[198:199] op_sel_hi:[1,0,1]
	v_pk_fma_f32 v[196:197], v[236:237], v[242:243], v[196:197] op_sel_hi:[1,0,1]
	v_pk_fma_f32 v[198:199], v[238:239], v[242:243], v[198:199] op_sel_hi:[1,0,1]
	v_cvt_pk_f32_fp8_e32 v[224:225], v98
	v_cvt_pk_f32_fp8_sdwa v[226:227], v98 src0_sel:WORD_1
	v_cvt_pk_f32_fp8_e32 v[228:229], v106
	v_cvt_pk_f32_fp8_sdwa v[230:231], v106 src0_sel:WORD_1
	v_lshlrev_b32_e32 v200, 16, v116
	v_and_b32_e32 v201, 0xffff0000, v116
	v_lshlrev_b32_e32 v202, 16, v117
	v_and_b32_e32 v203, 0xffff0000, v117
	v_pk_fma_f32 v[200:201], v[224:225], v[240:241], v[200:201] op_sel_hi:[1,0,1]
	v_pk_fma_f32 v[202:203], v[226:227], v[240:241], v[202:203] op_sel_hi:[1,0,1]
	v_pk_fma_f32 v[200:201], v[228:229], v[242:243], v[200:201] op_sel_hi:[1,0,1]
	v_pk_fma_f32 v[202:203], v[230:231], v[242:243], v[202:203] op_sel_hi:[1,0,1]
	v_cvt_pk_f32_fp8_e32 v[232:233], v99
	v_cvt_pk_f32_fp8_sdwa v[234:235], v99 src0_sel:WORD_1
	v_cvt_pk_f32_fp8_e32 v[236:237], v107
	v_cvt_pk_f32_fp8_sdwa v[238:239], v107 src0_sel:WORD_1
	v_lshlrev_b32_e32 v204, 16, v118
	v_and_b32_e32 v205, 0xffff0000, v118
	v_lshlrev_b32_e32 v206, 16, v119
	v_and_b32_e32 v207, 0xffff0000, v119
	v_pk_fma_f32 v[204:205], v[232:233], v[240:241], v[204:205] op_sel_hi:[1,0,1]
	v_pk_fma_f32 v[206:207], v[234:235], v[240:241], v[206:207] op_sel_hi:[1,0,1]
	v_pk_fma_f32 v[204:205], v[236:237], v[242:243], v[204:205] op_sel_hi:[1,0,1]
	v_pk_fma_f32 v[206:207], v[238:239], v[242:243], v[206:207] op_sel_hi:[1,0,1]
	v_cvt_pk_f32_fp8_e32 v[224:225], v100
	v_cvt_pk_f32_fp8_sdwa v[226:227], v100 src0_sel:WORD_1
	v_cvt_pk_f32_fp8_e32 v[228:229], v108
	v_cvt_pk_f32_fp8_sdwa v[230:231], v108 src0_sel:WORD_1
	v_lshlrev_b32_e32 v208, 16, v120
	v_and_b32_e32 v209, 0xffff0000, v120
	v_lshlrev_b32_e32 v210, 16, v121
	v_and_b32_e32 v211, 0xffff0000, v121
	v_pk_fma_f32 v[208:209], v[224:225], v[240:241], v[208:209] op_sel_hi:[1,0,1]
	v_pk_fma_f32 v[210:211], v[226:227], v[240:241], v[210:211] op_sel_hi:[1,0,1]
	v_pk_fma_f32 v[208:209], v[228:229], v[242:243], v[208:209] op_sel_hi:[1,0,1]
	v_pk_fma_f32 v[210:211], v[230:231], v[242:243], v[210:211] op_sel_hi:[1,0,1]
	v_cvt_pk_f32_fp8_e32 v[232:233], v101
	v_cvt_pk_f32_fp8_sdwa v[234:235], v101 src0_sel:WORD_1
	v_cvt_pk_f32_fp8_e32 v[236:237], v109
	v_cvt_pk_f32_fp8_sdwa v[238:239], v109 src0_sel:WORD_1
	v_lshlrev_b32_e32 v212, 16, v122
	v_and_b32_e32 v213, 0xffff0000, v122
	v_lshlrev_b32_e32 v214, 16, v123
	v_and_b32_e32 v215, 0xffff0000, v123
	v_pk_fma_f32 v[212:213], v[232:233], v[240:241], v[212:213] op_sel_hi:[1,0,1]
	v_pk_fma_f32 v[214:215], v[234:235], v[240:241], v[214:215] op_sel_hi:[1,0,1]
	v_pk_fma_f32 v[212:213], v[236:237], v[242:243], v[212:213] op_sel_hi:[1,0,1]
	v_pk_fma_f32 v[214:215], v[238:239], v[242:243], v[214:215] op_sel_hi:[1,0,1]
	v_cvt_pk_f32_fp8_e32 v[224:225], v102
	v_cvt_pk_f32_fp8_sdwa v[226:227], v102 src0_sel:WORD_1
	v_cvt_pk_f32_fp8_e32 v[228:229], v110
	v_cvt_pk_f32_fp8_sdwa v[230:231], v110 src0_sel:WORD_1
	v_lshlrev_b32_e32 v216, 16, v124
	v_and_b32_e32 v217, 0xffff0000, v124
	v_lshlrev_b32_e32 v218, 16, v125
	v_and_b32_e32 v219, 0xffff0000, v125
	v_pk_fma_f32 v[216:217], v[224:225], v[240:241], v[216:217] op_sel_hi:[1,0,1]
	v_pk_fma_f32 v[218:219], v[226:227], v[240:241], v[218:219] op_sel_hi:[1,0,1]
	v_pk_fma_f32 v[216:217], v[228:229], v[242:243], v[216:217] op_sel_hi:[1,0,1]
	v_pk_fma_f32 v[218:219], v[230:231], v[242:243], v[218:219] op_sel_hi:[1,0,1]
	v_cvt_pk_f32_fp8_e32 v[232:233], v103
	v_cvt_pk_f32_fp8_sdwa v[234:235], v103 src0_sel:WORD_1
	v_cvt_pk_f32_fp8_e32 v[236:237], v111
	v_cvt_pk_f32_fp8_sdwa v[238:239], v111 src0_sel:WORD_1
	v_lshlrev_b32_e32 v220, 16, v126
	v_and_b32_e32 v221, 0xffff0000, v126
	v_lshlrev_b32_e32 v222, 16, v127
	v_and_b32_e32 v223, 0xffff0000, v127
	v_pk_fma_f32 v[220:221], v[232:233], v[240:241], v[220:221] op_sel_hi:[1,0,1]
	v_pk_fma_f32 v[222:223], v[234:235], v[240:241], v[222:223] op_sel_hi:[1,0,1]
	v_pk_fma_f32 v[220:221], v[236:237], v[242:243], v[220:221] op_sel_hi:[1,0,1]
	v_pk_fma_f32 v[222:223], v[238:239], v[242:243], v[222:223] op_sel_hi:[1,0,1]
	s_add_u32 s56, s64, 0x5000000
	s_addc_u32 s57, s65, 0
	s_add_u32 s58, s56, 0x1000
	s_addc_u32 s59, s57, 0
	global_store_dwordx4 v4, v[192:195], s[56:57]
	global_store_dwordx4 v4, v[196:199], s[56:57] offset:1024
	global_store_dwordx4 v4, v[200:203], s[56:57] offset:2048
	global_store_dwordx4 v4, v[204:207], s[56:57] offset:3072
	global_store_dwordx4 v4, v[208:211], s[58:59]
	global_store_dwordx4 v4, v[212:215], s[58:59] offset:1024
	global_store_dwordx4 v4, v[216:219], s[58:59] offset:2048
	global_store_dwordx4 v4, v[220:223], s[58:59] offset:3072
	s_waitcnt vmcnt(8)
	s_lshl_b32 s50, s23, 11
	s_add_u32 s50, s48, s50
	s_addc_u32 s51, s49, 0
	s_lshl_b32 s52, s31, 11
	s_add_u32 s52, s48, s52
	s_addc_u32 s53, s49, 0
	s_add_u32 s54, s62, 0x3800000
	s_addc_u32 s55, s63, 0
	global_load_dword v96, v2, s[50:51]
	global_load_dword v97, v2, s[50:51] offset:256
	global_load_dword v98, v2, s[50:51] offset:512
	global_load_dword v99, v2, s[50:51] offset:768
	global_load_dword v100, v2, s[50:51] offset:1024
	global_load_dword v101, v2, s[50:51] offset:1280
	global_load_dword v102, v2, s[50:51] offset:1536
	global_load_dword v103, v2, s[50:51] offset:1792
	global_load_dword v104, v2, s[52:53]
	global_load_dword v105, v2, s[52:53] offset:256
	global_load_dword v106, v2, s[52:53] offset:512
	global_load_dword v107, v2, s[52:53] offset:768
	global_load_dword v108, v2, s[52:53] offset:1024
	global_load_dword v109, v2, s[52:53] offset:1280
	global_load_dword v110, v2, s[52:53] offset:1536
	global_load_dword v111, v2, s[52:53] offset:1792
	global_load_dwordx2 v[112:113], v3, s[54:55]
	global_load_dwordx2 v[114:115], v3, s[54:55] offset:512
	global_load_dwordx2 v[116:117], v3, s[54:55] offset:1024
	global_load_dwordx2 v[118:119], v3, s[54:55] offset:1536
	global_load_dwordx2 v[120:121], v3, s[54:55] offset:2048
	global_load_dwordx2 v[122:123], v3, s[54:55] offset:2560
	global_load_dwordx2 v[124:125], v3, s[54:55] offset:3072
	global_load_dwordx2 v[126:127], v3, s[54:55] offset:3584
	v_mov_b32_e32 v240, s38
	v_mov_b32_e32 v242, s46
	v_cvt_pk_f32_fp8_e32 v[224:225], v64
	v_cvt_pk_f32_fp8_sdwa v[226:227], v64 src0_sel:WORD_1
	v_cvt_pk_f32_fp8_e32 v[228:229], v72
	v_cvt_pk_f32_fp8_sdwa v[230:231], v72 src0_sel:WORD_1
	v_lshlrev_b32_e32 v192, 16, v80
	v_and_b32_e32 v193, 0xffff0000, v80
	v_lshlrev_b32_e32 v194, 16, v81
	v_and_b32_e32 v195, 0xffff0000, v81
	v_pk_fma_f32 v[192:193], v[224:225], v[240:241], v[192:193] op_sel_hi:[1,0,1]
	v_pk_fma_f32 v[194:195], v[226:227], v[240:241], v[194:195] op_sel_hi:[1,0,1]
	v_pk_fma_f32 v[192:193], v[228:229], v[242:243], v[192:193] op_sel_hi:[1,0,1]
	v_pk_fma_f32 v[194:195], v[230:231], v[242:243], v[194:195] op_sel_hi:[1,0,1]
	v_cvt_pk_f32_fp8_e32 v[232:233], v65
	v_cvt_pk_f32_fp8_sdwa v[234:235], v65 src0_sel:WORD_1
	v_cvt_pk_f32_fp8_e32 v[236:237], v73
	v_cvt_pk_f32_fp8_sdwa v[238:239], v73 src0_sel:WORD_1
	v_lshlrev_b32_e32 v196, 16, v82
	v_and_b32_e32 v197, 0xffff0000, v82
	v_lshlrev_b32_e32 v198, 16, v83
	v_and_b32_e32 v199, 0xffff0000, v83
	v_pk_fma_f32 v[196:197], v[232:233], v[240:241], v[196:197] op_sel_hi:[1,0,1]
	v_pk_fma_f32 v[198:199], v[234:235], v[240:241], v[198:199] op_sel_hi:[1,0,1]
	v_pk_fma_f32 v[196:197], v[236:237], v[242:243], v[196:197] op_sel_hi:[1,0,1]
	v_pk_fma_f32 v[198:199], v[238:239], v[242:243], v[198:199] op_sel_hi:[1,0,1]
	v_cvt_pk_f32_fp8_e32 v[224:225], v66
	v_cvt_pk_f32_fp8_sdwa v[226:227], v66 src0_sel:WORD_1
	v_cvt_pk_f32_fp8_e32 v[228:229], v74
	v_cvt_pk_f32_fp8_sdwa v[230:231], v74 src0_sel:WORD_1
	v_lshlrev_b32_e32 v200, 16, v84
	v_and_b32_e32 v201, 0xffff0000, v84
	v_lshlrev_b32_e32 v202, 16, v85
	v_and_b32_e32 v203, 0xffff0000, v85
	v_pk_fma_f32 v[200:201], v[224:225], v[240:241], v[200:201] op_sel_hi:[1,0,1]
	v_pk_fma_f32 v[202:203], v[226:227], v[240:241], v[202:203] op_sel_hi:[1,0,1]
	v_pk_fma_f32 v[200:201], v[228:229], v[242:243], v[200:201] op_sel_hi:[1,0,1]
	v_pk_fma_f32 v[202:203], v[230:231], v[242:243], v[202:203] op_sel_hi:[1,0,1]
	v_cvt_pk_f32_fp8_e32 v[232:233], v67
	v_cvt_pk_f32_fp8_sdwa v[234:235], v67 src0_sel:WORD_1
	v_cvt_pk_f32_fp8_e32 v[236:237], v75
	v_cvt_pk_f32_fp8_sdwa v[238:239], v75 src0_sel:WORD_1
	v_lshlrev_b32_e32 v204, 16, v86
	v_and_b32_e32 v205, 0xffff0000, v86
	v_lshlrev_b32_e32 v206, 16, v87
	v_and_b32_e32 v207, 0xffff0000, v87
	v_pk_fma_f32 v[204:205], v[232:233], v[240:241], v[204:205] op_sel_hi:[1,0,1]
	v_pk_fma_f32 v[206:207], v[234:235], v[240:241], v[206:207] op_sel_hi:[1,0,1]
	v_pk_fma_f32 v[204:205], v[236:237], v[242:243], v[204:205] op_sel_hi:[1,0,1]
	v_pk_fma_f32 v[206:207], v[238:239], v[242:243], v[206:207] op_sel_hi:[1,0,1]
	v_cvt_pk_f32_fp8_e32 v[224:225], v68
	v_cvt_pk_f32_fp8_sdwa v[226:227], v68 src0_sel:WORD_1
	v_cvt_pk_f32_fp8_e32 v[228:229], v76
	v_cvt_pk_f32_fp8_sdwa v[230:231], v76 src0_sel:WORD_1
	v_lshlrev_b32_e32 v208, 16, v88
	v_and_b32_e32 v209, 0xffff0000, v88
	v_lshlrev_b32_e32 v210, 16, v89
	v_and_b32_e32 v211, 0xffff0000, v89
	v_pk_fma_f32 v[208:209], v[224:225], v[240:241], v[208:209] op_sel_hi:[1,0,1]
	v_pk_fma_f32 v[210:211], v[226:227], v[240:241], v[210:211] op_sel_hi:[1,0,1]
	v_pk_fma_f32 v[208:209], v[228:229], v[242:243], v[208:209] op_sel_hi:[1,0,1]
	v_pk_fma_f32 v[210:211], v[230:231], v[242:243], v[210:211] op_sel_hi:[1,0,1]
	v_cvt_pk_f32_fp8_e32 v[232:233], v69
	v_cvt_pk_f32_fp8_sdwa v[234:235], v69 src0_sel:WORD_1
	v_cvt_pk_f32_fp8_e32 v[236:237], v77
	v_cvt_pk_f32_fp8_sdwa v[238:239], v77 src0_sel:WORD_1
	v_lshlrev_b32_e32 v212, 16, v90
	v_and_b32_e32 v213, 0xffff0000, v90
	v_lshlrev_b32_e32 v214, 16, v91
	v_and_b32_e32 v215, 0xffff0000, v91
	v_pk_fma_f32 v[212:213], v[232:233], v[240:241], v[212:213] op_sel_hi:[1,0,1]
	v_pk_fma_f32 v[214:215], v[234:235], v[240:241], v[214:215] op_sel_hi:[1,0,1]
	v_pk_fma_f32 v[212:213], v[236:237], v[242:243], v[212:213] op_sel_hi:[1,0,1]
	v_pk_fma_f32 v[214:215], v[238:239], v[242:243], v[214:215] op_sel_hi:[1,0,1]
	v_cvt_pk_f32_fp8_e32 v[224:225], v70
	v_cvt_pk_f32_fp8_sdwa v[226:227], v70 src0_sel:WORD_1
	v_cvt_pk_f32_fp8_e32 v[228:229], v78
	v_cvt_pk_f32_fp8_sdwa v[230:231], v78 src0_sel:WORD_1
	v_lshlrev_b32_e32 v216, 16, v92
	v_and_b32_e32 v217, 0xffff0000, v92
	v_lshlrev_b32_e32 v218, 16, v93
	v_and_b32_e32 v219, 0xffff0000, v93
	v_pk_fma_f32 v[216:217], v[224:225], v[240:241], v[216:217] op_sel_hi:[1,0,1]
	v_pk_fma_f32 v[218:219], v[226:227], v[240:241], v[218:219] op_sel_hi:[1,0,1]
	v_pk_fma_f32 v[216:217], v[228:229], v[242:243], v[216:217] op_sel_hi:[1,0,1]
	v_pk_fma_f32 v[218:219], v[230:231], v[242:243], v[218:219] op_sel_hi:[1,0,1]
	v_cvt_pk_f32_fp8_e32 v[232:233], v71
	v_cvt_pk_f32_fp8_sdwa v[234:235], v71 src0_sel:WORD_1
	v_cvt_pk_f32_fp8_e32 v[236:237], v79
	v_cvt_pk_f32_fp8_sdwa v[238:239], v79 src0_sel:WORD_1
	v_lshlrev_b32_e32 v220, 16, v94
	v_and_b32_e32 v221, 0xffff0000, v94
	v_lshlrev_b32_e32 v222, 16, v95
	v_and_b32_e32 v223, 0xffff0000, v95
	v_pk_fma_f32 v[220:221], v[232:233], v[240:241], v[220:221] op_sel_hi:[1,0,1]
	v_pk_fma_f32 v[222:223], v[234:235], v[240:241], v[222:223] op_sel_hi:[1,0,1]
	v_pk_fma_f32 v[220:221], v[236:237], v[242:243], v[220:221] op_sel_hi:[1,0,1]
	v_pk_fma_f32 v[222:223], v[238:239], v[242:243], v[222:223] op_sel_hi:[1,0,1]
	s_add_u32 s56, s64, 0x6000000
	s_addc_u32 s57, s65, 0
	s_add_u32 s58, s56, 0x1000
	s_addc_u32 s59, s57, 0
	global_store_dwordx4 v4, v[192:195], s[56:57]
	global_store_dwordx4 v4, v[196:199], s[56:57] offset:1024
	global_store_dwordx4 v4, v[200:203], s[56:57] offset:2048
	global_store_dwordx4 v4, v[204:207], s[56:57] offset:3072
	global_store_dwordx4 v4, v[208:211], s[58:59]
	global_store_dwordx4 v4, v[212:215], s[58:59] offset:1024
	global_store_dwordx4 v4, v[216:219], s[58:59] offset:2048
	global_store_dwordx4 v4, v[220:223], s[58:59] offset:3072
	s_waitcnt vmcnt(8)
	v_mov_b32_e32 v240, s39
	v_mov_b32_e32 v242, s47
	v_cvt_pk_f32_fp8_e32 v[224:225], v96
	v_cvt_pk_f32_fp8_sdwa v[226:227], v96 src0_sel:WORD_1
	v_cvt_pk_f32_fp8_e32 v[228:229], v104
	v_cvt_pk_f32_fp8_sdwa v[230:231], v104 src0_sel:WORD_1
	v_lshlrev_b32_e32 v192, 16, v112
	v_and_b32_e32 v193, 0xffff0000, v112
	v_lshlrev_b32_e32 v194, 16, v113
	v_and_b32_e32 v195, 0xffff0000, v113
	v_pk_fma_f32 v[192:193], v[224:225], v[240:241], v[192:193] op_sel_hi:[1,0,1]
	v_pk_fma_f32 v[194:195], v[226:227], v[240:241], v[194:195] op_sel_hi:[1,0,1]
	v_pk_fma_f32 v[192:193], v[228:229], v[242:243], v[192:193] op_sel_hi:[1,0,1]
	v_pk_fma_f32 v[194:195], v[230:231], v[242:243], v[194:195] op_sel_hi:[1,0,1]
	v_cvt_pk_f32_fp8_e32 v[232:233], v97
	v_cvt_pk_f32_fp8_sdwa v[234:235], v97 src0_sel:WORD_1
	v_cvt_pk_f32_fp8_e32 v[236:237], v105
	v_cvt_pk_f32_fp8_sdwa v[238:239], v105 src0_sel:WORD_1
	v_lshlrev_b32_e32 v196, 16, v114
	v_and_b32_e32 v197, 0xffff0000, v114
	v_lshlrev_b32_e32 v198, 16, v115
	v_and_b32_e32 v199, 0xffff0000, v115
	v_pk_fma_f32 v[196:197], v[232:233], v[240:241], v[196:197] op_sel_hi:[1,0,1]
	v_pk_fma_f32 v[198:199], v[234:235], v[240:241], v[198:199] op_sel_hi:[1,0,1]
	v_pk_fma_f32 v[196:197], v[236:237], v[242:243], v[196:197] op_sel_hi:[1,0,1]
	v_pk_fma_f32 v[198:199], v[238:239], v[242:243], v[198:199] op_sel_hi:[1,0,1]
	v_cvt_pk_f32_fp8_e32 v[224:225], v98
	v_cvt_pk_f32_fp8_sdwa v[226:227], v98 src0_sel:WORD_1
	v_cvt_pk_f32_fp8_e32 v[228:229], v106
	v_cvt_pk_f32_fp8_sdwa v[230:231], v106 src0_sel:WORD_1
	v_lshlrev_b32_e32 v200, 16, v116
	v_and_b32_e32 v201, 0xffff0000, v116
	v_lshlrev_b32_e32 v202, 16, v117
	v_and_b32_e32 v203, 0xffff0000, v117
	v_pk_fma_f32 v[200:201], v[224:225], v[240:241], v[200:201] op_sel_hi:[1,0,1]
	v_pk_fma_f32 v[202:203], v[226:227], v[240:241], v[202:203] op_sel_hi:[1,0,1]
	v_pk_fma_f32 v[200:201], v[228:229], v[242:243], v[200:201] op_sel_hi:[1,0,1]
	v_pk_fma_f32 v[202:203], v[230:231], v[242:243], v[202:203] op_sel_hi:[1,0,1]
	v_cvt_pk_f32_fp8_e32 v[232:233], v99
	v_cvt_pk_f32_fp8_sdwa v[234:235], v99 src0_sel:WORD_1
	v_cvt_pk_f32_fp8_e32 v[236:237], v107
	v_cvt_pk_f32_fp8_sdwa v[238:239], v107 src0_sel:WORD_1
	v_lshlrev_b32_e32 v204, 16, v118
	v_and_b32_e32 v205, 0xffff0000, v118
	v_lshlrev_b32_e32 v206, 16, v119
	v_and_b32_e32 v207, 0xffff0000, v119
	v_pk_fma_f32 v[204:205], v[232:233], v[240:241], v[204:205] op_sel_hi:[1,0,1]
	v_pk_fma_f32 v[206:207], v[234:235], v[240:241], v[206:207] op_sel_hi:[1,0,1]
	v_pk_fma_f32 v[204:205], v[236:237], v[242:243], v[204:205] op_sel_hi:[1,0,1]
	v_pk_fma_f32 v[206:207], v[238:239], v[242:243], v[206:207] op_sel_hi:[1,0,1]
	v_cvt_pk_f32_fp8_e32 v[224:225], v100
	v_cvt_pk_f32_fp8_sdwa v[226:227], v100 src0_sel:WORD_1
	v_cvt_pk_f32_fp8_e32 v[228:229], v108
	v_cvt_pk_f32_fp8_sdwa v[230:231], v108 src0_sel:WORD_1
	v_lshlrev_b32_e32 v208, 16, v120
	v_and_b32_e32 v209, 0xffff0000, v120
	v_lshlrev_b32_e32 v210, 16, v121
	v_and_b32_e32 v211, 0xffff0000, v121
	v_pk_fma_f32 v[208:209], v[224:225], v[240:241], v[208:209] op_sel_hi:[1,0,1]
	v_pk_fma_f32 v[210:211], v[226:227], v[240:241], v[210:211] op_sel_hi:[1,0,1]
	v_pk_fma_f32 v[208:209], v[228:229], v[242:243], v[208:209] op_sel_hi:[1,0,1]
	v_pk_fma_f32 v[210:211], v[230:231], v[242:243], v[210:211] op_sel_hi:[1,0,1]
	v_cvt_pk_f32_fp8_e32 v[232:233], v101
	v_cvt_pk_f32_fp8_sdwa v[234:235], v101 src0_sel:WORD_1
	v_cvt_pk_f32_fp8_e32 v[236:237], v109
	v_cvt_pk_f32_fp8_sdwa v[238:239], v109 src0_sel:WORD_1
	v_lshlrev_b32_e32 v212, 16, v122
	v_and_b32_e32 v213, 0xffff0000, v122
	v_lshlrev_b32_e32 v214, 16, v123
	v_and_b32_e32 v215, 0xffff0000, v123
	v_pk_fma_f32 v[212:213], v[232:233], v[240:241], v[212:213] op_sel_hi:[1,0,1]
	v_pk_fma_f32 v[214:215], v[234:235], v[240:241], v[214:215] op_sel_hi:[1,0,1]
	v_pk_fma_f32 v[212:213], v[236:237], v[242:243], v[212:213] op_sel_hi:[1,0,1]
	v_pk_fma_f32 v[214:215], v[238:239], v[242:243], v[214:215] op_sel_hi:[1,0,1]
	v_cvt_pk_f32_fp8_e32 v[224:225], v102
	v_cvt_pk_f32_fp8_sdwa v[226:227], v102 src0_sel:WORD_1
	v_cvt_pk_f32_fp8_e32 v[228:229], v110
	v_cvt_pk_f32_fp8_sdwa v[230:231], v110 src0_sel:WORD_1
	v_lshlrev_b32_e32 v216, 16, v124
	v_and_b32_e32 v217, 0xffff0000, v124
	v_lshlrev_b32_e32 v218, 16, v125
	v_and_b32_e32 v219, 0xffff0000, v125
	v_pk_fma_f32 v[216:217], v[224:225], v[240:241], v[216:217] op_sel_hi:[1,0,1]
	v_pk_fma_f32 v[218:219], v[226:227], v[240:241], v[218:219] op_sel_hi:[1,0,1]
	v_pk_fma_f32 v[216:217], v[228:229], v[242:243], v[216:217] op_sel_hi:[1,0,1]
	v_pk_fma_f32 v[218:219], v[230:231], v[242:243], v[218:219] op_sel_hi:[1,0,1]
	v_cvt_pk_f32_fp8_e32 v[232:233], v103
	v_cvt_pk_f32_fp8_sdwa v[234:235], v103 src0_sel:WORD_1
	v_cvt_pk_f32_fp8_e32 v[236:237], v111
	v_cvt_pk_f32_fp8_sdwa v[238:239], v111 src0_sel:WORD_1
	v_lshlrev_b32_e32 v220, 16, v126
	v_and_b32_e32 v221, 0xffff0000, v126
	v_lshlrev_b32_e32 v222, 16, v127
	v_and_b32_e32 v223, 0xffff0000, v127
	v_pk_fma_f32 v[220:221], v[232:233], v[240:241], v[220:221] op_sel_hi:[1,0,1]
	v_pk_fma_f32 v[222:223], v[234:235], v[240:241], v[222:223] op_sel_hi:[1,0,1]
	v_pk_fma_f32 v[220:221], v[236:237], v[242:243], v[220:221] op_sel_hi:[1,0,1]
	v_pk_fma_f32 v[222:223], v[238:239], v[242:243], v[222:223] op_sel_hi:[1,0,1]
	s_add_u32 s56, s64, 0x7000000
	s_addc_u32 s57, s65, 0
	s_add_u32 s58, s56, 0x1000
	s_addc_u32 s59, s57, 0
	global_store_dwordx4 v4, v[192:195], s[56:57]
	global_store_dwordx4 v4, v[196:199], s[56:57] offset:1024
	global_store_dwordx4 v4, v[200:203], s[56:57] offset:2048
	global_store_dwordx4 v4, v[204:207], s[56:57] offset:3072
	global_store_dwordx4 v4, v[208:211], s[58:59]
	global_store_dwordx4 v4, v[212:215], s[58:59] offset:1024
	global_store_dwordx4 v4, v[216:219], s[58:59] offset:2048
	global_store_dwordx4 v4, v[220:223], s[58:59] offset:3072
